# baseline (speedup 1.0000x reference)
.LBB2_2:
	s_waitcnt lgkmcnt(1)
	v_and_b32_e32 v109, v108, v107
	v_cmp_ne_u32_e32 vcc, 0, v109
	s_cbranch_vccz .LBB2_4
	s_nop 0
	v_lshrrev_b64 v[108:109], v0, vcc
	v_cmp_ne_u32_e64 s[0:1], 0, v108
	v_cndmask_b32_e64 v109, 0, 1, vcc
	v_add_u32_e32 v119, v119, v109
	v_addc_co_u32_e64 v105, s[0:1], 0, v105, s[0:1]
	s_branch .LBB2_2

.LBB2_8:
	s_waitcnt lgkmcnt(2)
	v_and_b32_e32 v109, v108, v107
	v_cmp_ne_u32_e32 vcc, 0, v109
	s_cbranch_vccz .LBB2_10
	s_nop 0
	v_lshrrev_b64 v[108:109], v0, vcc
	v_cmp_ne_u32_e64 s[4:5], 0, v108
	v_cndmask_b32_e64 v109, 0, 1, vcc
	v_add_u32_e32 v117, v117, v109
	v_addc_co_u32_e64 v120, s[4:5], 0, v120, s[4:5]
	s_branch .LBB2_8
